# accumulator zeroing per GEMM unit: 128 v_mov replaced by 2 f32 MFMA (0*0+0, 32 regs each) + 32 v_mov_b64
# baseline (speedup 1.0000x reference)
.LBB0_143:
	s_ashr_i32 s45, s44, 31
	s_lshl_b64 s[38:39], s[44:45], 19
	s_add_u32 s50, s31, s38
	s_addc_u32 s51, s33, s39
	s_and_b64 s[38:39], s[46:47], exec
	s_cselect_b32 s5, s51, s3
	s_cselect_b32 s45, s50, s2
	s_ashr_i32 s43, s42, 31
	s_lshl_b64 s[38:39], s[42:43], 19
	s_add_u32 s52, s35, s38
	s_addc_u32 s53, s37, s39
	s_and_b64 s[38:39], s[46:47], exec
	s_cselect_b32 s43, s53, s63
	s_cselect_b32 s72, s52, s62
	s_add_u32 s2, s2, 0x40080
	s_addc_u32 s3, s3, 0
	s_add_u32 s62, s62, 0x100
	s_addc_u32 s63, s63, 0
	s_mov_b32 s73, -2
	v_mov_b32_e32 v130, 0
	s_nop 1
	v_mfma_f32_32x32x1_2b_f32 v[2:33], v130, v130, 0
	v_mov_b64_e32 v[66:67], 0
	v_mov_b64_e32 v[68:69], 0
	v_mov_b64_e32 v[70:71], 0
	v_mov_b64_e32 v[72:73], 0
	v_mov_b64_e32 v[74:75], 0
	v_mov_b64_e32 v[76:77], 0
	v_mov_b64_e32 v[78:79], 0
	v_mov_b64_e32 v[80:81], 0
	v_mov_b64_e32 v[82:83], 0
	v_mov_b64_e32 v[84:85], 0
	v_mov_b64_e32 v[86:87], 0
	v_mov_b64_e32 v[88:89], 0
	v_mov_b64_e32 v[90:91], 0
	v_mov_b64_e32 v[92:93], 0
	v_mov_b64_e32 v[94:95], 0
	v_mov_b64_e32 v[96:97], 0
	v_mfma_f32_32x32x1_2b_f32 v[34:65], v130, v130, 0
	v_mov_b64_e32 v[98:99], 0
	v_mov_b64_e32 v[100:101], 0
	v_mov_b64_e32 v[102:103], 0
	v_mov_b64_e32 v[104:105], 0
	v_mov_b64_e32 v[106:107], 0
	v_mov_b64_e32 v[108:109], 0
	v_mov_b64_e32 v[110:111], 0
	v_mov_b64_e32 v[112:113], 0
	v_mov_b64_e32 v[114:115], 0
	v_mov_b64_e32 v[116:117], 0
	v_mov_b64_e32 v[118:119], 0
	v_mov_b64_e32 v[120:121], 0
	v_mov_b64_e32 v[122:123], 0
	v_mov_b64_e32 v[124:125], 0
	v_mov_b64_e32 v[126:127], 0
	v_mov_b64_e32 v[128:129], 0

.LBB0_591:
	s_ashr_i32 s11, s10, 31
	s_lshl_b64 s[24:25], s[10:11], 19
	s_add_u32 s24, s36, s24
	s_addc_u32 s25, s37, s25
	s_and_b64 s[30:31], s[30:31], exec
	s_cselect_b32 s11, s25, s29
	s_cselect_b32 s62, s24, s28
	s_add_u32 s63, s28, 0x100
	s_addc_u32 s72, s29, 0
	s_mov_b32 s73, -2
	v_mov_b32_e32 v144, 0
	s_nop 1
	v_mfma_f32_32x32x1_2b_f32 v[2:33], v144, v144, 0
	v_mov_b64_e32 v[66:67], 0
	v_mov_b64_e32 v[68:69], 0
	v_mov_b64_e32 v[70:71], 0
	v_mov_b64_e32 v[72:73], 0
	v_mov_b64_e32 v[74:75], 0
	v_mov_b64_e32 v[76:77], 0
	v_mov_b64_e32 v[78:79], 0
	v_mov_b64_e32 v[80:81], 0
	v_mov_b64_e32 v[82:83], 0
	v_mov_b64_e32 v[84:85], 0
	v_mov_b64_e32 v[86:87], 0
	v_mov_b64_e32 v[88:89], 0
	v_mov_b64_e32 v[90:91], 0
	v_mov_b64_e32 v[92:93], 0
	v_mov_b64_e32 v[94:95], 0
	v_mov_b64_e32 v[96:97], 0
	v_mfma_f32_32x32x1_2b_f32 v[34:65], v144, v144, 0
	v_mov_b64_e32 v[98:99], 0
	v_mov_b64_e32 v[100:101], 0
	v_mov_b64_e32 v[102:103], 0
	v_mov_b64_e32 v[104:105], 0
	v_mov_b64_e32 v[106:107], 0
	v_mov_b64_e32 v[108:109], 0
	v_mov_b64_e32 v[110:111], 0
	v_mov_b64_e32 v[112:113], 0
	v_mov_b64_e32 v[114:115], 0
	v_mov_b64_e32 v[116:117], 0
	v_mov_b64_e32 v[118:119], 0
	v_mov_b64_e32 v[120:121], 0
	v_mov_b64_e32 v[122:123], 0
	v_mov_b64_e32 v[124:125], 0
	v_mov_b64_e32 v[126:127], 0
	v_mov_b64_e32 v[128:129], 0

.LBB0_653:
	s_ashr_i32 s11, s10, 31
	s_lshl_b64 s[22:23], s[10:11], 19
	s_add_u32 s22, s35, s22
	s_addc_u32 s23, s36, s23
	s_and_b64 s[24:25], s[30:31], exec
	s_cselect_b32 s11, s23, s27
	s_cselect_b32 s62, s22, s26
	s_ashr_i32 s21, s20, 31
	s_lshl_b64 s[24:25], s[20:21], 19
	s_add_u32 s24, s37, s24
	s_addc_u32 s25, s38, s25
	s_and_b64 s[30:31], s[30:31], exec
	s_cselect_b32 s21, s25, s29
	s_cselect_b32 s63, s24, s28
	s_add_u32 s26, s26, 0x40080
	s_addc_u32 s27, s27, 0
	s_add_u32 s72, s28, 0x100
	s_addc_u32 s73, s29, 0
	s_mov_b32 s74, -2
	v_mov_b32_e32 v152, 0
	s_nop 1
	v_mfma_f32_32x32x1_2b_f32 v[2:33], v152, v152, 0
	v_mov_b64_e32 v[66:67], 0
	v_mov_b64_e32 v[68:69], 0
	v_mov_b64_e32 v[70:71], 0
	v_mov_b64_e32 v[72:73], 0
	v_mov_b64_e32 v[74:75], 0
	v_mov_b64_e32 v[76:77], 0
	v_mov_b64_e32 v[78:79], 0
	v_mov_b64_e32 v[80:81], 0
	v_mov_b64_e32 v[82:83], 0
	v_mov_b64_e32 v[84:85], 0
	v_mov_b64_e32 v[86:87], 0
	v_mov_b64_e32 v[88:89], 0
	v_mov_b64_e32 v[90:91], 0
	v_mov_b64_e32 v[92:93], 0
	v_mov_b64_e32 v[94:95], 0
	v_mov_b64_e32 v[96:97], 0
	v_mfma_f32_32x32x1_2b_f32 v[34:65], v152, v152, 0
	v_mov_b64_e32 v[98:99], 0
	v_mov_b64_e32 v[100:101], 0
	v_mov_b64_e32 v[102:103], 0
	v_mov_b64_e32 v[104:105], 0
	v_mov_b64_e32 v[106:107], 0
	v_mov_b64_e32 v[108:109], 0
	v_mov_b64_e32 v[110:111], 0
	v_mov_b64_e32 v[112:113], 0
	v_mov_b64_e32 v[114:115], 0
	v_mov_b64_e32 v[116:117], 0
	v_mov_b64_e32 v[118:119], 0
	v_mov_b64_e32 v[120:121], 0
	v_mov_b64_e32 v[122:123], 0
	v_mov_b64_e32 v[124:125], 0
	v_mov_b64_e32 v[126:127], 0
	v_mov_b64_e32 v[128:129], 0

.LBB0_695:
	s_mov_b32 s1, s27
	s_mov_b32 s10, s0
	s_mov_b32 s21, s0
	s_mov_b32 s29, s0
	s_or_b64 s[10:11], s[20:21], s[10:11]
	s_or_b64 s[20:21], s[28:29], s[0:1]
	s_add_u32 s1, s24, 0x100
	s_addc_u32 s81, s25, 0
	s_add_u32 s22, s22, 0x58080
	s_addc_u32 s23, s23, 0
	s_mov_b32 s82, -2
	v_mov_b32_e32 v146, 0
	s_nop 1
	v_mfma_f32_32x32x1_2b_f32 v[2:33], v146, v146, 0
	v_mov_b64_e32 v[66:67], 0
	v_mov_b64_e32 v[68:69], 0
	v_mov_b64_e32 v[70:71], 0
	v_mov_b64_e32 v[72:73], 0
	v_mov_b64_e32 v[74:75], 0
	v_mov_b64_e32 v[76:77], 0
	v_mov_b64_e32 v[78:79], 0
	v_mov_b64_e32 v[80:81], 0
	v_mov_b64_e32 v[82:83], 0
	v_mov_b64_e32 v[84:85], 0
	v_mov_b64_e32 v[86:87], 0
	v_mov_b64_e32 v[88:89], 0
	v_mov_b64_e32 v[90:91], 0
	v_mov_b64_e32 v[92:93], 0
	v_mov_b64_e32 v[94:95], 0
	v_mov_b64_e32 v[96:97], 0
	v_mfma_f32_32x32x1_2b_f32 v[34:65], v146, v146, 0
	v_mov_b64_e32 v[98:99], 0
	v_mov_b64_e32 v[100:101], 0
	v_mov_b64_e32 v[102:103], 0
	v_mov_b64_e32 v[104:105], 0
	v_mov_b64_e32 v[106:107], 0
	v_mov_b64_e32 v[108:109], 0
	v_mov_b64_e32 v[110:111], 0
	v_mov_b64_e32 v[112:113], 0
	v_mov_b64_e32 v[114:115], 0
	v_mov_b64_e32 v[116:117], 0
	v_mov_b64_e32 v[118:119], 0
	v_mov_b64_e32 v[120:121], 0
	v_mov_b64_e32 v[122:123], 0
	v_mov_b64_e32 v[124:125], 0
	v_mov_b64_e32 v[126:127], 0
	v_mov_b64_e32 v[128:129], 0

.LBB0_757:
	s_ashr_i32 s37, s36, 31
	s_lshl_b64 s[2:3], s[36:37], 19
	s_add_u32 s46, s21, s2
	s_addc_u32 s47, s23, s3
	s_and_b64 s[2:3], s[44:45], exec
	s_cselect_b32 s37, s47, s39
	s_cselect_b32 s52, s46, s38
	s_ashr_i32 s35, s34, 31
	s_lshl_b64 s[2:3], s[34:35], 19
	s_add_u32 s50, s25, s2
	s_addc_u32 s51, s27, s3
	s_and_b64 s[2:3], s[44:45], exec
	s_cselect_b32 s35, s51, s5
	s_cselect_b32 s53, s50, s4
	s_add_u32 s2, s38, 0x40080
	s_addc_u32 s3, s39, 0
	s_add_u32 s74, s4, 0x100
	s_addc_u32 s75, s5, 0
	s_mov_b32 s81, -2
	v_mov_b32_e32 v130, 0
	s_nop 1
	v_mfma_f32_32x32x1_2b_f32 v[2:33], v130, v130, 0
	v_mov_b64_e32 v[66:67], 0
	v_mov_b64_e32 v[68:69], 0
	v_mov_b64_e32 v[70:71], 0
	v_mov_b64_e32 v[72:73], 0
	v_mov_b64_e32 v[74:75], 0
	v_mov_b64_e32 v[76:77], 0
	v_mov_b64_e32 v[78:79], 0
	v_mov_b64_e32 v[80:81], 0
	v_mov_b64_e32 v[82:83], 0
	v_mov_b64_e32 v[84:85], 0
	v_mov_b64_e32 v[86:87], 0
	v_mov_b64_e32 v[88:89], 0
	v_mov_b64_e32 v[90:91], 0
	v_mov_b64_e32 v[92:93], 0
	v_mov_b64_e32 v[94:95], 0
	v_mov_b64_e32 v[96:97], 0
	v_mfma_f32_32x32x1_2b_f32 v[34:65], v130, v130, 0
	v_mov_b64_e32 v[98:99], 0
	v_mov_b64_e32 v[100:101], 0
	v_mov_b64_e32 v[102:103], 0
	v_mov_b64_e32 v[104:105], 0
	v_mov_b64_e32 v[106:107], 0
	v_mov_b64_e32 v[108:109], 0
	v_mov_b64_e32 v[110:111], 0
	v_mov_b64_e32 v[112:113], 0
	v_mov_b64_e32 v[114:115], 0
	v_mov_b64_e32 v[116:117], 0
	v_mov_b64_e32 v[118:119], 0
	v_mov_b64_e32 v[120:121], 0
	v_mov_b64_e32 v[122:123], 0
	v_mov_b64_e32 v[124:125], 0
	v_mov_b64_e32 v[126:127], 0
	v_mov_b64_e32 v[128:129], 0

.LBB0_1204:
	s_ashr_i32 s11, s10, 31
	s_lshl_b64 s[16:17], s[10:11], 19
	s_add_u32 s16, s27, s16
	s_addc_u32 s17, s28, s17
	s_and_b64 s[22:23], s[22:23], exec
	s_cselect_b32 s11, s17, s21
	s_cselect_b32 s44, s16, s20
	s_add_u32 s45, s20, 0x100
	s_addc_u32 s46, s21, 0
	s_mov_b32 s47, -2
	v_mov_b32_e32 v144, 0
	s_nop 1
	v_mfma_f32_32x32x1_2b_f32 v[2:33], v144, v144, 0
	v_mov_b64_e32 v[66:67], 0
	v_mov_b64_e32 v[68:69], 0
	v_mov_b64_e32 v[70:71], 0
	v_mov_b64_e32 v[72:73], 0
	v_mov_b64_e32 v[74:75], 0
	v_mov_b64_e32 v[76:77], 0
	v_mov_b64_e32 v[78:79], 0
	v_mov_b64_e32 v[80:81], 0
	v_mov_b64_e32 v[82:83], 0
	v_mov_b64_e32 v[84:85], 0
	v_mov_b64_e32 v[86:87], 0
	v_mov_b64_e32 v[88:89], 0
	v_mov_b64_e32 v[90:91], 0
	v_mov_b64_e32 v[92:93], 0
	v_mov_b64_e32 v[94:95], 0
	v_mov_b64_e32 v[96:97], 0
	v_mfma_f32_32x32x1_2b_f32 v[34:65], v144, v144, 0
	v_mov_b64_e32 v[98:99], 0
	v_mov_b64_e32 v[100:101], 0
	v_mov_b64_e32 v[102:103], 0
	v_mov_b64_e32 v[104:105], 0
	v_mov_b64_e32 v[106:107], 0
	v_mov_b64_e32 v[108:109], 0
	v_mov_b64_e32 v[110:111], 0
	v_mov_b64_e32 v[112:113], 0
	v_mov_b64_e32 v[114:115], 0
	v_mov_b64_e32 v[116:117], 0
	v_mov_b64_e32 v[118:119], 0
	v_mov_b64_e32 v[120:121], 0
	v_mov_b64_e32 v[122:123], 0
	v_mov_b64_e32 v[124:125], 0
	v_mov_b64_e32 v[126:127], 0
	v_mov_b64_e32 v[128:129], 0

.LBB0_1338:
	s_mov_b32 s38, s50
	s_mov_b32 s41, s50
	s_or_b64 s[88:89], s[40:41], s[38:39]
	v_readfirstlane_b32 s38, v4
	s_mov_b32 s39, s50
	s_or_b64 s[90:91], s[38:39], s[50:51]
	s_add_u32 s38, s92, 0x100
	s_addc_u32 s39, s93, 0
	s_add_u32 s92, s78, 0x70080
	s_addc_u32 s93, s79, 0
	s_mov_b32 s40, -2
	v_mov_b32_e32 v132, 0
	s_nop 1
	v_mfma_f32_32x32x1_2b_f32 v[2:33], v132, v132, 0
	v_mov_b64_e32 v[66:67], 0
	v_mov_b64_e32 v[68:69], 0
	v_mov_b64_e32 v[70:71], 0
	v_mov_b64_e32 v[72:73], 0
	v_mov_b64_e32 v[74:75], 0
	v_mov_b64_e32 v[76:77], 0
	v_mov_b64_e32 v[78:79], 0
	v_mov_b64_e32 v[80:81], 0
	v_mov_b64_e32 v[82:83], 0
	v_mov_b64_e32 v[84:85], 0
	v_mov_b64_e32 v[86:87], 0
	v_mov_b64_e32 v[88:89], 0
	v_mov_b64_e32 v[90:91], 0
	v_mov_b64_e32 v[92:93], 0
	v_mov_b64_e32 v[94:95], 0
	v_mov_b64_e32 v[96:97], 0
	v_mfma_f32_32x32x1_2b_f32 v[34:65], v132, v132, 0
	v_mov_b64_e32 v[98:99], 0
	v_mov_b64_e32 v[100:101], 0
	v_mov_b64_e32 v[102:103], 0
	v_mov_b64_e32 v[104:105], 0
	v_mov_b64_e32 v[106:107], 0
	v_mov_b64_e32 v[108:109], 0
	v_mov_b64_e32 v[110:111], 0
	v_mov_b64_e32 v[112:113], 0
	v_mov_b64_e32 v[114:115], 0
	v_mov_b64_e32 v[116:117], 0
	v_mov_b64_e32 v[118:119], 0
	v_mov_b64_e32 v[120:121], 0
	v_mov_b64_e32 v[122:123], 0
	v_mov_b64_e32 v[124:125], 0
	v_mov_b64_e32 v[126:127], 0
	v_mov_b64_e32 v[128:129], 0

.LBB0_1386:
	s_mov_b32 s90, s95
	s_ashr_i32 s91, s95, 31
	s_lshl_b64 s[38:39], s[90:91], 18
	s_mov_b32 s75, s40
	s_add_u32 s40, s22, s38
	s_mov_b32 s21, s41
	s_addc_u32 s41, s23, s39
	s_and_b64 s[38:39], s[92:93], exec
	s_mov_b32 s44, s94
	s_cselect_b32 s94, s40, s78
	s_cselect_b32 s95, s41, s79
	s_cmp_lg_u32 s21, s96
	s_cselect_b64 s[38:39], -1, 0
	s_cmp_lg_u32 s44, s97
	s_cselect_b64 s[40:41], -1, 0
	s_or_b64 s[96:97], s[38:39], s[40:41]
	s_lshl_b32 s38, s21, 15
	s_lshl_b32 s39, s44, 8
	s_add_i32 s39, s39, s38
	v_add_u32_e32 v2, s39, v206
	v_add_u32_e32 v4, s39, v210
	v_ashrrev_i32_e32 v3, 31, v2
	v_ashrrev_i32_e32 v5, 31, v4
	s_add_u32 s91, s78, 0x100
	s_mov_b32 s74, s76
	v_lshl_add_u64 v[196:197], v[2:3], 2, s[56:57]
	v_lshl_add_u64 v[198:199], v[4:5], 2, s[56:57]
	s_addc_u32 s46, s79, 0
	s_mov_b32 s88, -2
	s_mov_b64 s[78:79], 0
	v_mov_b32_e32 v2, 0
	s_nop 1
	v_mfma_f32_32x32x1_2b_f32 v[66:97], v2, v2, 0
	v_mov_b64_e32 v[130:131], 0
	v_mov_b64_e32 v[132:133], 0
	v_mov_b64_e32 v[134:135], 0
	v_mov_b64_e32 v[136:137], 0
	v_mov_b64_e32 v[138:139], 0
	v_mov_b64_e32 v[140:141], 0
	v_mov_b64_e32 v[142:143], 0
	v_mov_b64_e32 v[144:145], 0
	v_mov_b64_e32 v[146:147], 0
	v_mov_b64_e32 v[148:149], 0
	v_mov_b64_e32 v[150:151], 0
	v_mov_b64_e32 v[152:153], 0
	v_mov_b64_e32 v[154:155], 0
	v_mov_b64_e32 v[156:157], 0
	v_mov_b64_e32 v[158:159], 0
	v_mov_b64_e32 v[160:161], 0
	v_mfma_f32_32x32x1_2b_f32 v[98:129], v2, v2, 0
	v_mov_b64_e32 v[162:163], 0
	v_mov_b64_e32 v[164:165], 0
	v_mov_b64_e32 v[166:167], 0
	v_mov_b64_e32 v[168:169], 0
	v_mov_b64_e32 v[170:171], 0
	v_mov_b64_e32 v[172:173], 0
	v_mov_b64_e32 v[174:175], 0
	v_mov_b64_e32 v[176:177], 0
	v_mov_b64_e32 v[178:179], 0
	v_mov_b64_e32 v[180:181], 0
	v_mov_b64_e32 v[182:183], 0
	v_mov_b64_e32 v[184:185], 0
	v_mov_b64_e32 v[186:187], 0
	v_mov_b64_e32 v[188:189], 0
	v_mov_b64_e32 v[190:191], 0
	v_mov_b64_e32 v[192:193], 0
